# opt6 + rope cos/sin preload in both input-projection epilogues (IN0, IN1)
# baseline (speedup 1.0000x reference)
.LBB0_87:
	ds_read_b128 v[144:147], v160
	ds_read_b128 v[164:167], v160 offset:1024
	ds_read_b128 v[168:171], v160 offset:2048
	ds_read_b128 v[172:175], v160 offset:3072
	s_add_u32 s36, s34, 0xfffc0080
	s_addc_u32 s37, s35, -1
	s_cmp_eq_u32 s58, 12
	s_cselect_b32 s41, s3, s37
	s_cselect_b32 s40, s7, s36
	s_cselect_b32 s37, s15, s57
	s_cselect_b32 s36, s17, s56
	v_lshl_add_u64 v[148:149], s[34:35], 0, v[136:137]
	s_add_i32 m0, s43, 0xc000
	ds_read_b128 v[176:179], v161
	ds_read_b128 v[180:183], v161 offset:1024
	ds_read_b128 v[184:187], v161 offset:2048
	ds_read_b128 v[188:191], v161 offset:3072
	ds_read_b128 v[192:195], v161 offset:4096
	ds_read_b128 v[196:199], v161 offset:5120
	ds_read_b128 v[200:203], v161 offset:6144
	ds_read_b128 v[204:207], v161 offset:7168
	global_load_lds_dwordx4 v[148:149], off
	v_lshl_add_u64 v[148:149], s[34:35], 0, v[138:139]
	s_add_i32 m0, s43, 0xe000
	s_nop 0
	global_load_lds_dwordx4 v[148:149], off
	s_waitcnt lgkmcnt(8)
	s_barrier
	s_waitcnt lgkmcnt(0)
	s_setprio 1
	s_waitcnt lgkmcnt(0)
	v_mfma_f32_16x16x32_bf16 v[124:127], v[144:147], v[176:179], v[124:127]
	v_mfma_f32_16x16x32_bf16 v[120:123], v[168:171], v[176:179], v[120:123]
	v_mfma_f32_16x16x32_bf16 v[108:111], v[144:147], v[184:187], v[108:111]
	v_mfma_f32_16x16x32_bf16 v[104:107], v[168:171], v[184:187], v[104:107]
	v_mfma_f32_16x16x32_bf16 v[92:95], v[144:147], v[192:195], v[92:95]
	v_mfma_f32_16x16x32_bf16 v[88:91], v[168:171], v[192:195], v[88:91]
	v_mfma_f32_16x16x32_bf16 v[76:79], v[144:147], v[200:203], v[76:79]
	v_mfma_f32_16x16x32_bf16 v[72:75], v[168:171], v[200:203], v[72:75]
	v_mfma_f32_16x16x32_bf16 v[124:127], v[164:167], v[180:183], v[124:127]
	v_mfma_f32_16x16x32_bf16 v[120:123], v[172:175], v[180:183], v[120:123]
	v_mfma_f32_16x16x32_bf16 v[108:111], v[164:167], v[188:191], v[108:111]
	v_mfma_f32_16x16x32_bf16 v[104:107], v[172:175], v[188:191], v[104:107]
	v_mfma_f32_16x16x32_bf16 v[92:95], v[164:167], v[196:199], v[92:95]
	v_mfma_f32_16x16x32_bf16 v[88:91], v[172:175], v[196:199], v[88:91]
	v_mfma_f32_16x16x32_bf16 v[76:79], v[164:167], v[204:207], v[76:79]
	v_mfma_f32_16x16x32_bf16 v[72:75], v[172:175], v[204:207], v[72:75]
	s_setprio 0
	s_barrier
	s_add_i32 s59, s53, s42
	v_lshl_add_u64 v[148:149], s[36:37], 0, v[128:129]
	s_mov_b32 m0, s59
	ds_read_b128 v[208:211], v162
	ds_read_b128 v[212:215], v162 offset:1024
	ds_read_b128 v[216:219], v162 offset:2048
	ds_read_b128 v[220:223], v162 offset:3072
	global_load_lds_dwordx4 v[148:149], off
	v_lshl_add_u64 v[224:225], s[36:37], 0, v[130:131]
	s_add_i32 m0, s59, 0x2000
	s_nop 0
	global_load_lds_dwordx4 v[224:225], off
	s_barrier
	s_waitcnt lgkmcnt(0)
	s_setprio 1
	s_waitcnt lgkmcnt(0)
	v_mfma_f32_16x16x32_bf16 v[116:119], v[208:211], v[176:179], v[116:119]
	v_mfma_f32_16x16x32_bf16 v[112:115], v[216:219], v[176:179], v[112:115]
	v_mfma_f32_16x16x32_bf16 v[100:103], v[208:211], v[184:187], v[100:103]
	v_mfma_f32_16x16x32_bf16 v[96:99], v[216:219], v[184:187], v[96:99]
	v_mfma_f32_16x16x32_bf16 v[84:87], v[208:211], v[192:195], v[84:87]
	v_mfma_f32_16x16x32_bf16 v[80:83], v[216:219], v[192:195], v[80:83]
	v_mfma_f32_16x16x32_bf16 v[68:71], v[208:211], v[200:203], v[68:71]
	v_mfma_f32_16x16x32_bf16 v[64:67], v[216:219], v[200:203], v[64:67]
	v_mfma_f32_16x16x32_bf16 v[116:119], v[212:215], v[180:183], v[116:119]
	v_mfma_f32_16x16x32_bf16 v[112:115], v[220:223], v[180:183], v[112:115]
	v_mfma_f32_16x16x32_bf16 v[100:103], v[212:215], v[188:191], v[100:103]
	v_mfma_f32_16x16x32_bf16 v[96:99], v[220:223], v[188:191], v[96:99]
	v_mfma_f32_16x16x32_bf16 v[84:87], v[212:215], v[196:199], v[84:87]
	v_mfma_f32_16x16x32_bf16 v[80:83], v[220:223], v[196:199], v[80:83]
	v_mfma_f32_16x16x32_bf16 v[68:71], v[212:215], v[204:207], v[68:71]
	v_mfma_f32_16x16x32_bf16 v[64:67], v[220:223], v[204:207], v[64:67]
	s_setprio 0
	s_mov_b32 m0, s43
	v_lshl_add_u64 v[226:227], s[40:41], 0, v[128:129]
	s_barrier
	ds_read_b128 v[176:179], v161 offset:16384
	ds_read_b128 v[180:183], v161 offset:17408
	ds_read_b128 v[184:187], v161 offset:18432
	ds_read_b128 v[188:191], v161 offset:19456
	ds_read_b128 v[192:195], v161 offset:20480
	ds_read_b128 v[196:199], v161 offset:21504
	ds_read_b128 v[200:203], v161 offset:22528
	ds_read_b128 v[204:207], v161 offset:23552
	global_load_lds_dwordx4 v[226:227], off
	v_lshl_add_u64 v[228:229], s[40:41], 0, v[130:131]
	s_mov_b32 m0, s44
	s_nop 0
	global_load_lds_dwordx4 v[228:229], off
	s_barrier
	s_waitcnt lgkmcnt(0)
	s_setprio 1
	s_waitcnt lgkmcnt(0)
	v_mfma_f32_16x16x32_bf16 v[60:63], v[144:147], v[176:179], v[60:63]
	v_mfma_f32_16x16x32_bf16 v[56:59], v[168:171], v[176:179], v[56:59]
	v_mfma_f32_16x16x32_bf16 v[44:47], v[144:147], v[184:187], v[44:47]
	v_mfma_f32_16x16x32_bf16 v[40:43], v[168:171], v[184:187], v[40:43]
	v_mfma_f32_16x16x32_bf16 v[28:31], v[144:147], v[192:195], v[28:31]
	v_mfma_f32_16x16x32_bf16 v[24:27], v[168:171], v[192:195], v[24:27]
	v_mfma_f32_16x16x32_bf16 v[12:15], v[144:147], v[200:203], v[12:15]
	v_mfma_f32_16x16x32_bf16 v[8:11], v[168:171], v[200:203], v[8:11]
	v_mfma_f32_16x16x32_bf16 v[60:63], v[164:167], v[180:183], v[60:63]
	v_mfma_f32_16x16x32_bf16 v[56:59], v[172:175], v[180:183], v[56:59]
	v_mfma_f32_16x16x32_bf16 v[44:47], v[164:167], v[188:191], v[44:47]
	v_mfma_f32_16x16x32_bf16 v[40:43], v[172:175], v[188:191], v[40:43]
	v_mfma_f32_16x16x32_bf16 v[28:31], v[164:167], v[196:199], v[28:31]
	v_mfma_f32_16x16x32_bf16 v[24:27], v[172:175], v[196:199], v[24:27]
	v_mfma_f32_16x16x32_bf16 v[12:15], v[164:167], v[204:207], v[12:15]
	v_mfma_f32_16x16x32_bf16 v[8:11], v[172:175], v[204:207], v[8:11]
	s_setprio 0
	s_barrier
	s_add_u32 s60, s36, 0x40000
	s_addc_u32 s61, s37, 0
	s_add_i32 s59, s54, s42
	v_lshl_add_u64 v[144:145], s[60:61], 0, v[128:129]
	s_mov_b32 m0, s59
	s_nop 0
	global_load_lds_dwordx4 v[144:145], off
	v_lshl_add_u64 v[144:145], s[60:61], 0, v[130:131]
	s_add_i32 m0, s59, 0x2000
	s_nop 0
	global_load_lds_dwordx4 v[144:145], off
	s_waitcnt vmcnt(6)
	s_barrier
	s_setprio 1
	v_mfma_f32_16x16x32_bf16 v[52:55], v[208:211], v[176:179], v[52:55]
	v_mfma_f32_16x16x32_bf16 v[48:51], v[216:219], v[176:179], v[48:51]
	v_mfma_f32_16x16x32_bf16 v[36:39], v[208:211], v[184:187], v[36:39]
	v_mfma_f32_16x16x32_bf16 v[32:35], v[216:219], v[184:187], v[32:35]
	v_mfma_f32_16x16x32_bf16 v[20:23], v[208:211], v[192:195], v[20:23]
	v_mfma_f32_16x16x32_bf16 v[16:19], v[216:219], v[192:195], v[16:19]
	v_mfma_f32_16x16x32_bf16 v[4:7], v[208:211], v[200:203], v[4:7]
	v_mfma_f32_16x16x32_bf16 v[0:3], v[216:219], v[200:203], v[0:3]
	v_mfma_f32_16x16x32_bf16 v[52:55], v[212:215], v[180:183], v[52:55]
	v_mfma_f32_16x16x32_bf16 v[48:51], v[220:223], v[180:183], v[48:51]
	v_mfma_f32_16x16x32_bf16 v[36:39], v[212:215], v[188:191], v[36:39]
	v_mfma_f32_16x16x32_bf16 v[32:35], v[220:223], v[188:191], v[32:35]
	v_mfma_f32_16x16x32_bf16 v[20:23], v[212:215], v[196:199], v[20:23]
	v_mfma_f32_16x16x32_bf16 v[16:19], v[220:223], v[196:199], v[16:19]
	v_mfma_f32_16x16x32_bf16 v[4:7], v[212:215], v[204:207], v[4:7]
	v_mfma_f32_16x16x32_bf16 v[0:3], v[220:223], v[204:207], v[0:3]
	s_setprio 0
	s_add_i32 s59, 0, 0x18000
	v_add_u32_e32 v163, s59, v151
	s_barrier
	ds_read_b128 v[144:147], v163
	ds_read_b128 v[164:167], v163 offset:1024
	ds_read_b128 v[168:171], v163 offset:2048
	ds_read_b128 v[172:175], v163 offset:3072
	s_add_u32 s40, s40, 0x40000
	s_addc_u32 s41, s41, 0
	s_mov_b32 m0, s45
	v_lshl_add_u64 v[208:209], s[40:41], 0, v[128:129]
	ds_read_b128 v[176:179], v161 offset:32768
	ds_read_b128 v[180:183], v161 offset:33792
	ds_read_b128 v[184:187], v161 offset:34816
	ds_read_b128 v[188:191], v161 offset:35840
	ds_read_b128 v[192:195], v161 offset:36864
	ds_read_b128 v[196:199], v161 offset:37888
	ds_read_b128 v[200:203], v161 offset:38912
	ds_read_b128 v[204:207], v161 offset:39936
	global_load_lds_dwordx4 v[208:209], off
	v_lshl_add_u64 v[208:209], s[40:41], 0, v[130:131]
	s_mov_b32 m0, s46
	s_nop 0
	global_load_lds_dwordx4 v[208:209], off
	s_waitcnt lgkmcnt(8)
	s_barrier
	s_waitcnt lgkmcnt(0)
	s_setprio 1
	s_waitcnt lgkmcnt(0)
	v_mfma_f32_16x16x32_bf16 v[124:127], v[144:147], v[176:179], v[124:127]
	v_mfma_f32_16x16x32_bf16 v[120:123], v[168:171], v[176:179], v[120:123]
	v_mfma_f32_16x16x32_bf16 v[108:111], v[144:147], v[184:187], v[108:111]
	v_mfma_f32_16x16x32_bf16 v[104:107], v[168:171], v[184:187], v[104:107]
	v_mfma_f32_16x16x32_bf16 v[92:95], v[144:147], v[192:195], v[92:95]
	v_mfma_f32_16x16x32_bf16 v[88:91], v[168:171], v[192:195], v[88:91]
	v_mfma_f32_16x16x32_bf16 v[76:79], v[144:147], v[200:203], v[76:79]
	v_mfma_f32_16x16x32_bf16 v[72:75], v[168:171], v[200:203], v[72:75]
	v_mfma_f32_16x16x32_bf16 v[124:127], v[164:167], v[180:183], v[124:127]
	v_mfma_f32_16x16x32_bf16 v[120:123], v[172:175], v[180:183], v[120:123]
	v_mfma_f32_16x16x32_bf16 v[108:111], v[164:167], v[188:191], v[108:111]
	v_mfma_f32_16x16x32_bf16 v[104:107], v[172:175], v[188:191], v[104:107]
	v_mfma_f32_16x16x32_bf16 v[92:95], v[164:167], v[196:199], v[92:95]
	v_mfma_f32_16x16x32_bf16 v[88:91], v[172:175], v[196:199], v[88:91]
	v_mfma_f32_16x16x32_bf16 v[76:79], v[164:167], v[204:207], v[76:79]
	v_mfma_f32_16x16x32_bf16 v[72:75], v[172:175], v[204:207], v[72:75]
	s_setprio 0
	s_barrier
	s_add_i32 s40, 0, 0x1c000
	s_add_i32 s41, s59, s42
	v_add_u32_e32 v163, s40, v151
	v_lshl_add_u64 v[148:149], v[148:149], 0, s[10:11]
	s_mov_b32 m0, s41
	ds_read_b128 v[208:211], v163
	ds_read_b128 v[212:215], v163 offset:1024
	ds_read_b128 v[216:219], v163 offset:2048
	ds_read_b128 v[220:223], v163 offset:3072
	global_load_lds_dwordx4 v[148:149], off
	v_lshl_add_u64 v[148:149], v[224:225], 0, s[10:11]
	s_add_i32 m0, s41, 0x2000
	s_nop 0
	global_load_lds_dwordx4 v[148:149], off
	s_barrier
	s_waitcnt lgkmcnt(0)
	s_setprio 1
	s_waitcnt lgkmcnt(0)
	v_mfma_f32_16x16x32_bf16 v[116:119], v[208:211], v[176:179], v[116:119]
	v_mfma_f32_16x16x32_bf16 v[112:115], v[216:219], v[176:179], v[112:115]
	v_mfma_f32_16x16x32_bf16 v[100:103], v[208:211], v[184:187], v[100:103]
	v_mfma_f32_16x16x32_bf16 v[96:99], v[216:219], v[184:187], v[96:99]
	v_mfma_f32_16x16x32_bf16 v[84:87], v[208:211], v[192:195], v[84:87]
	v_mfma_f32_16x16x32_bf16 v[80:83], v[216:219], v[192:195], v[80:83]
	v_mfma_f32_16x16x32_bf16 v[68:71], v[208:211], v[200:203], v[68:71]
	v_mfma_f32_16x16x32_bf16 v[64:67], v[216:219], v[200:203], v[64:67]
	v_mfma_f32_16x16x32_bf16 v[116:119], v[212:215], v[180:183], v[116:119]
	v_mfma_f32_16x16x32_bf16 v[112:115], v[220:223], v[180:183], v[112:115]
	v_mfma_f32_16x16x32_bf16 v[100:103], v[212:215], v[188:191], v[100:103]
	v_mfma_f32_16x16x32_bf16 v[96:99], v[220:223], v[188:191], v[96:99]
	v_mfma_f32_16x16x32_bf16 v[84:87], v[212:215], v[196:199], v[84:87]
	v_mfma_f32_16x16x32_bf16 v[80:83], v[220:223], v[196:199], v[80:83]
	v_mfma_f32_16x16x32_bf16 v[68:71], v[212:215], v[204:207], v[68:71]
	v_mfma_f32_16x16x32_bf16 v[64:67], v[220:223], v[204:207], v[64:67]
	s_setprio 0
	s_mov_b32 m0, s49
	v_lshl_add_u64 v[148:149], v[226:227], 0, s[10:11]
	s_barrier
	ds_read_b128 v[176:179], v161 offset:49152
	ds_read_b128 v[180:183], v161 offset:50176
	ds_read_b128 v[184:187], v161 offset:51200
	ds_read_b128 v[188:191], v161 offset:52224
	ds_read_b128 v[192:195], v161 offset:53248
	ds_read_b128 v[196:199], v161 offset:54272
	ds_read_b128 v[200:203], v161 offset:55296
	ds_read_b128 v[204:207], v161 offset:56320
	global_load_lds_dwordx4 v[148:149], off
	v_lshl_add_u64 v[148:149], v[228:229], 0, s[10:11]
	s_mov_b32 m0, s50
	s_nop 0
	global_load_lds_dwordx4 v[148:149], off
	s_barrier
	s_waitcnt lgkmcnt(0)
	s_setprio 1
	s_waitcnt lgkmcnt(0)
	v_mfma_f32_16x16x32_bf16 v[60:63], v[144:147], v[176:179], v[60:63]
	v_mfma_f32_16x16x32_bf16 v[56:59], v[168:171], v[176:179], v[56:59]
	v_mfma_f32_16x16x32_bf16 v[44:47], v[144:147], v[184:187], v[44:47]
	v_mfma_f32_16x16x32_bf16 v[40:43], v[168:171], v[184:187], v[40:43]
	v_mfma_f32_16x16x32_bf16 v[28:31], v[144:147], v[192:195], v[28:31]
	v_mfma_f32_16x16x32_bf16 v[24:27], v[168:171], v[192:195], v[24:27]
	v_mfma_f32_16x16x32_bf16 v[12:15], v[144:147], v[200:203], v[12:15]
	v_mfma_f32_16x16x32_bf16 v[8:11], v[168:171], v[200:203], v[8:11]
	v_mfma_f32_16x16x32_bf16 v[60:63], v[164:167], v[180:183], v[60:63]
	v_mfma_f32_16x16x32_bf16 v[56:59], v[172:175], v[180:183], v[56:59]
	v_mfma_f32_16x16x32_bf16 v[44:47], v[164:167], v[188:191], v[44:47]
	v_mfma_f32_16x16x32_bf16 v[40:43], v[172:175], v[188:191], v[40:43]
	v_mfma_f32_16x16x32_bf16 v[28:31], v[164:167], v[196:199], v[28:31]
	v_mfma_f32_16x16x32_bf16 v[24:27], v[172:175], v[196:199], v[24:27]
	v_mfma_f32_16x16x32_bf16 v[12:15], v[164:167], v[204:207], v[12:15]
	v_mfma_f32_16x16x32_bf16 v[8:11], v[172:175], v[204:207], v[8:11]
	s_setprio 0
	s_barrier
	s_add_u32 s36, s36, 0x40080
	s_addc_u32 s37, s37, 0
	s_add_i32 s40, s40, s42
	v_lshl_add_u64 v[144:145], s[36:37], 0, v[128:129]
	s_mov_b32 m0, s40
	s_nop 0
	global_load_lds_dwordx4 v[144:145], off
	v_lshl_add_u64 v[144:145], s[36:37], 0, v[130:131]
	s_add_i32 m0, s40, 0x2000
	s_nop 0
	global_load_lds_dwordx4 v[144:145], off
	s_waitcnt vmcnt(6)
	s_barrier
	s_setprio 1
	v_mfma_f32_16x16x32_bf16 v[52:55], v[208:211], v[176:179], v[52:55]
	v_mfma_f32_16x16x32_bf16 v[48:51], v[216:219], v[176:179], v[48:51]
	v_mfma_f32_16x16x32_bf16 v[36:39], v[208:211], v[184:187], v[36:39]
	v_mfma_f32_16x16x32_bf16 v[32:35], v[216:219], v[184:187], v[32:35]
	v_mfma_f32_16x16x32_bf16 v[20:23], v[208:211], v[192:195], v[20:23]
	v_mfma_f32_16x16x32_bf16 v[16:19], v[216:219], v[192:195], v[16:19]
	v_mfma_f32_16x16x32_bf16 v[4:7], v[208:211], v[200:203], v[4:7]
	v_mfma_f32_16x16x32_bf16 v[0:3], v[216:219], v[200:203], v[0:3]
	v_mfma_f32_16x16x32_bf16 v[52:55], v[212:215], v[180:183], v[52:55]
	v_mfma_f32_16x16x32_bf16 v[48:51], v[220:223], v[180:183], v[48:51]
	v_mfma_f32_16x16x32_bf16 v[36:39], v[212:215], v[188:191], v[36:39]
	v_mfma_f32_16x16x32_bf16 v[32:35], v[220:223], v[188:191], v[32:35]
	v_mfma_f32_16x16x32_bf16 v[20:23], v[212:215], v[196:199], v[20:23]
	v_mfma_f32_16x16x32_bf16 v[16:19], v[220:223], v[196:199], v[16:19]
	v_mfma_f32_16x16x32_bf16 v[4:7], v[212:215], v[204:207], v[4:7]
	v_mfma_f32_16x16x32_bf16 v[0:3], v[220:223], v[204:207], v[0:3]
	s_setprio 0
	s_add_i32 s58, s58, 2
	s_add_u32 s34, s34, 0x100
	s_addc_u32 s35, s35, 0
	s_add_u32 s56, s56, 0x100
	s_addc_u32 s57, s57, 0
	s_cmp_gt_u32 s58, 13
	s_barrier
	s_cbranch_scc0 .LBB0_87
	s_lshl_b32 s17, s6, 8
	v_add_u32_e32 v145, s17, v150
	s_lshl_b32 s15, s2, 8
	v_lshlrev_b32_e32 v146, 4, v145
	v_lshlrev_b32_e32 v178, 6, v145
	v_mov_b32_e32 v179, 0
	v_lshl_add_u64 v[178:179], v[178:179], 0, v[134:135]
	v_lshlrev_b32_e32 v230, 6, v145
	v_add_u32_e32 v230, 0x2000, v230
	v_mov_b32_e32 v231, 0
	v_lshl_add_u64 v[230:231], v[230:231], 0, v[134:135]
	global_load_dwordx4 v[180:183], v[178:179], off offset:0
	global_load_dwordx4 v[184:187], v[178:179], off offset:32
	global_load_dwordx4 v[188:191], v[178:179], off offset:1024
	global_load_dwordx4 v[192:195], v[178:179], off offset:1056
	global_load_dwordx4 v[196:199], v[178:179], off offset:2048
	global_load_dwordx4 v[200:203], v[178:179], off offset:2080
	global_load_dwordx4 v[204:207], v[178:179], off offset:3072
	global_load_dwordx4 v[208:211], v[178:179], off offset:3104
	global_load_dwordx4 v[212:215], v[230:231], off offset:0
	global_load_dwordx4 v[216:219], v[230:231], off offset:32
	global_load_dwordx4 v[220:223], v[230:231], off offset:1024
	global_load_dwordx4 v[232:235], v[230:231], off offset:1056
	global_load_dwordx4 v[236:239], v[230:231], off offset:2048
	global_load_dwordx4 v[240:243], v[230:231], off offset:2080
	global_load_dwordx4 v[244:247], v[230:231], off offset:3072
	global_load_dwordx4 v[248:251], v[230:231], off offset:3104
	s_waitcnt vmcnt(0)
	v_or_b32_e32 v144, s15, v152
	v_cndmask_b32_e64 v148, 0, 1, s[12:13]
	v_ashrrev_i32_e32 v147, 31, v146
	v_cmp_ne_u32_e64 s[6:7], 1, v148
	s_andn2_b64 vcc, exec, s[12:13]
	v_cmp_gt_i32_e64 s[2:3], s47, v144
	s_cbranch_vccnz .LBB0_92
	s_add_i32 s34, s15, 0xfffffa00
	s_cmpk_lt_u32 s34, 0x280
	s_cselect_b64 s[34:35], -1, 0
	s_or_b64 s[34:35], s[2:3], s[34:35]
	s_and_saveexec_b64 s[2:3], s[34:35]
	s_cbranch_execz .LBB0_91
	v_lshl_add_u64 v[148:149], v[146:147], 2, v[134:135]
	v_mov_b32_e32 v174, v126
	v_mov_b32_e32 v175, v126
	v_mov_b32_e32 v149, v124
	v_mov_b32_e32 v163, v124
	v_mov_b32_e32 v172, v125
	v_mov_b32_e32 v173, v125
	v_mov_b32_e32 v176, v127
	v_mov_b32_e32 v177, v127
	v_mov_b32_e32 v148, v127
	s_nop 1
	v_permlane32_swap_b32 v175, v174
	s_nop 1
	v_permlane32_swap_b32 v163, v149
	s_nop 1
	v_permlane32_swap_b32 v173, v172
	s_nop 1
	v_permlane32_swap_b32 v177, v176
	v_mov_b32_e32 v168, v180
	v_mov_b32_e32 v169, v181
	v_mov_b32_e32 v170, v182
	v_mov_b32_e32 v171, v183
	v_mov_b32_e32 v164, v184
	v_mov_b32_e32 v165, v185
	v_mov_b32_e32 v166, v186
	v_mov_b32_e32 v167, v187
	v_mul_f32_e32 v126, v126, v170
	v_cndmask_b32_e64 v127, v174, v175, s[0:1]
	v_cndmask_b32_e64 v174, v176, v177, s[0:1]
	v_mul_f32_e32 v127, v132, v127
	v_cndmask_b32_e64 v173, v172, v173, s[0:1]
	v_cndmask_b32_e64 v172, v149, v163, s[0:1]
	v_mul_f32_e32 v149, v132, v174
	v_mul_f32_e32 v170, v166, v127
	v_mov_b32_e32 v166, v171
	v_pk_mul_f32 v[172:173], v[132:133], v[172:173]
	v_pk_mul_f32 v[148:149], v[148:149], v[166:167]
	v_pk_mul_f32 v[164:165], v[164:165], v[172:173]
	v_mov_b32_e32 v127, v148
	v_mov_b32_e32 v171, v149
	v_pk_fma_f32 v[124:125], v[124:125], v[168:169], v[164:165]
	v_pk_add_f32 v[126:127], v[126:127], v[170:171]

.LBB0_92:
	v_readlane_b32 s2, v253, 22
	v_readlane_b32 s3, v253, 23
	v_cvt_pk_bf16_f32 v120, v120, v121
	v_cvt_pk_bf16_f32 v121, v122, v123
	v_mov_b64_e32 v[148:149], s[2:3]
	v_mad_i64_i32 v[148:149], s[2:3], v145, s55, v[148:149]
	v_ashrrev_i32_e32 v145, 31, v144
	v_lshl_add_u64 v[148:149], v[144:145], 1, v[148:149]
	global_store_dwordx2 v[148:149], v[120:121], off offset:32
	v_or_b32_e32 v120, 0x80, v144
	v_cvt_pk_bf16_f32 v124, v124, v125
	v_cvt_pk_bf16_f32 v125, v126, v127
	s_and_b64 vcc, exec, s[6:7]
	v_cmp_gt_i32_e64 s[2:3], s47, v120
	global_store_dwordx2 v[148:149], v[124:125], off
	s_cbranch_vccnz .LBB0_96
	s_add_i32 s34, s15, 0xfffffa80
	s_cmpk_lt_u32 s34, 0x280
	s_cselect_b64 s[34:35], -1, 0
	s_or_b64 s[34:35], s[2:3], s[34:35]
	s_and_saveexec_b64 s[2:3], s[34:35]
	s_cbranch_execz .LBB0_95
	v_lshl_add_u64 v[126:127], v[146:147], 2, v[134:135]
	v_mov_b32_e32 v146, v117
	v_mov_b32_e32 v147, v117
	v_mov_b32_e32 v121, v116
	v_mov_b32_e32 v127, v116
	v_mov_b32_e32 v163, v118
	v_mov_b32_e32 v168, v118
	s_nop 1
	v_permlane32_swap_b32 v147, v146
	v_mov_b32_e32 v169, v119
	v_mov_b32_e32 v170, v119
	v_mov_b32_e32 v126, v119
	s_nop 1
	v_permlane32_swap_b32 v127, v121
	s_nop 1
	v_permlane32_swap_b32 v168, v163
	v_cndmask_b32_e64 v147, v146, v147, s[0:1]
	v_cndmask_b32_e64 v119, v163, v168, s[0:1]
	v_cndmask_b32_e64 v146, v121, v127, s[0:1]
	s_nop 1
	v_permlane32_swap_b32 v170, v169
	v_pk_mul_f32 v[146:147], v[132:133], v[146:147]
	v_cndmask_b32_e64 v163, v169, v170, s[0:1]
	v_mul_f32_e32 v119, v132, v119
	v_mul_f32_e32 v127, v132, v163
	v_mov_b32_e32 v164, v180
	v_mov_b32_e32 v165, v181
	v_mov_b32_e32 v166, v182
	v_mov_b32_e32 v167, v183
	v_mov_b32_e32 v122, v184
	v_mov_b32_e32 v123, v185
	v_mov_b32_e32 v124, v186
	v_mov_b32_e32 v125, v187
	v_pk_mul_f32 v[122:123], v[122:123], v[146:147]
	v_mul_f32_e32 v146, v124, v119
	v_mov_b32_e32 v124, v167
	v_pk_mul_f32 v[124:125], v[126:127], v[124:125]
	v_mul_f32_e32 v118, v118, v166
	v_mov_b32_e32 v119, v124
	v_mov_b32_e32 v147, v125
	v_pk_fma_f32 v[116:117], v[116:117], v[164:165], v[122:123]
	v_pk_add_f32 v[118:119], v[118:119], v[146:147]

.LBB0_96:
	v_cvt_pk_bf16_f32 v112, v112, v113
	v_cvt_pk_bf16_f32 v113, v114, v115
	v_add_u32_e32 v114, s17, v153
	global_store_dwordx2 v[148:149], v[112:113], off offset:288
	v_lshlrev_b32_e32 v112, 4, v114
	v_cvt_pk_bf16_f32 v116, v116, v117
	v_cvt_pk_bf16_f32 v117, v118, v119
	s_and_b64 vcc, exec, s[6:7]
	v_ashrrev_i32_e32 v113, 31, v112
	global_store_dwordx2 v[148:149], v[116:117], off offset:256
	s_cbranch_vccnz .LBB0_100
	s_add_i32 s2, s15, 0xfffffa00
	s_cmpk_lt_u32 s2, 0x280
	v_cmp_gt_i32_e32 vcc, s47, v144
	s_cselect_b64 s[2:3], -1, 0
	s_or_b64 s[34:35], vcc, s[2:3]
	s_and_saveexec_b64 s[2:3], s[34:35]
	s_cbranch_execz .LBB0_99
	v_lshl_add_u64 v[122:123], v[112:113], 2, v[134:135]
	s_nop 0
	v_mov_b32_e32 v147, v110
	v_mov_b32_e32 v148, v110
	v_mov_b32_e32 v127, v109
	v_mov_b32_e32 v146, v109
	v_mov_b32_e32 v149, v111
	v_mov_b32_e32 v163, v111
	v_mov_b32_e32 v126, v111
	s_nop 1
	v_permlane32_swap_b32 v147, v148
	v_mov_b32_e32 v115, v108
	v_cndmask_b32_e64 v111, v148, v147, s[0:1]
	v_mov_b32_e32 v121, v108
	s_nop 1
	v_permlane32_swap_b32 v127, v146
	s_nop 1
	v_permlane32_swap_b32 v149, v163
	v_mul_f32_e32 v111, v132, v111
	v_cndmask_b32_e64 v148, v163, v149, s[0:1]
	s_nop 1
	v_permlane32_swap_b32 v115, v121
	v_cndmask_b32_e64 v147, v146, v127, s[0:1]
	v_cndmask_b32_e64 v146, v121, v115, s[0:1]
	v_mul_f32_e32 v127, v132, v148
	v_pk_mul_f32 v[146:147], v[132:133], v[146:147]
	v_mov_b32_e32 v122, v188
	v_mov_b32_e32 v123, v189
	v_mov_b32_e32 v124, v190
	v_mov_b32_e32 v125, v191
	v_mov_b32_e32 v116, v192
	v_mov_b32_e32 v117, v193
	v_mov_b32_e32 v118, v194
	v_mov_b32_e32 v119, v195
	v_mul_f32_e32 v110, v110, v124
	v_mul_f32_e32 v124, v118, v111
	v_mov_b32_e32 v118, v125
	v_pk_mul_f32 v[118:119], v[126:127], v[118:119]
	v_pk_mul_f32 v[116:117], v[116:117], v[146:147]
	v_mov_b32_e32 v111, v118
	v_mov_b32_e32 v125, v119
	v_pk_fma_f32 v[108:109], v[108:109], v[122:123], v[116:117]
	v_pk_add_f32 v[110:111], v[110:111], v[124:125]

.LBB0_100:
	v_readlane_b32 s2, v253, 22
	v_readlane_b32 s3, v253, 23
	v_cvt_pk_bf16_f32 v108, v108, v109
	v_cvt_pk_bf16_f32 v109, v110, v111
	v_mov_b64_e32 v[116:117], s[2:3]
	v_mad_i64_i32 v[114:115], s[2:3], v114, s55, v[116:117]
	v_lshl_add_u64 v[114:115], v[144:145], 1, v[114:115]
	v_cvt_pk_bf16_f32 v104, v104, v105
	v_cvt_pk_bf16_f32 v105, v106, v107
	s_and_b64 vcc, exec, s[6:7]
	global_store_dwordx2 v[114:115], v[108:109], off
	global_store_dwordx2 v[114:115], v[104:105], off offset:32
	s_cbranch_vccnz .LBB0_104
	s_add_i32 s2, s15, 0xfffffa80
	s_cmpk_lt_u32 s2, 0x280
	v_cmp_gt_i32_e32 vcc, s47, v120
	s_cselect_b64 s[2:3], -1, 0
	s_or_b64 s[34:35], vcc, s[2:3]
	s_and_saveexec_b64 s[2:3], s[34:35]
	s_cbranch_execz .LBB0_103
	v_lshl_add_u64 v[108:109], v[112:113], 2, v[134:135]
	s_nop 0
	v_mov_b32_e32 v119, v102
	v_mov_b32_e32 v121, v102
	v_mov_b32_e32 v113, v100
	v_mov_b32_e32 v116, v100
	v_mov_b32_e32 v117, v101
	v_mov_b32_e32 v118, v101
	v_mov_b32_e32 v122, v103
	v_mov_b32_e32 v123, v103
	v_mov_b32_e32 v112, v103
	s_nop 1
	v_permlane32_swap_b32 v119, v121
	s_nop 1
	v_permlane32_swap_b32 v113, v116
	s_nop 1
	v_permlane32_swap_b32 v117, v118
	s_nop 1
	v_permlane32_swap_b32 v122, v123
	v_mov_b32_e32 v108, v188
	v_mov_b32_e32 v109, v189
	v_mov_b32_e32 v110, v190
	v_mov_b32_e32 v111, v191
	v_mov_b32_e32 v104, v192
	v_mov_b32_e32 v105, v193
	v_mov_b32_e32 v106, v194
	v_mov_b32_e32 v107, v195
	v_mul_f32_e32 v102, v102, v110
	v_cndmask_b32_e64 v103, v121, v119, s[0:1]
	v_cndmask_b32_e64 v119, v123, v122, s[0:1]
	v_mul_f32_e32 v103, v132, v103
	v_cndmask_b32_e64 v117, v118, v117, s[0:1]
	v_cndmask_b32_e64 v116, v116, v113, s[0:1]
	v_mul_f32_e32 v113, v132, v119
	v_mul_f32_e32 v110, v106, v103
	v_mov_b32_e32 v106, v111
	v_pk_mul_f32 v[116:117], v[132:133], v[116:117]
	v_pk_mul_f32 v[106:107], v[112:113], v[106:107]
	v_pk_mul_f32 v[104:105], v[104:105], v[116:117]
	v_mov_b32_e32 v103, v106
	v_mov_b32_e32 v111, v107
	v_pk_fma_f32 v[100:101], v[100:101], v[108:109], v[104:105]
	v_pk_add_f32 v[102:103], v[102:103], v[110:111]

.LBB0_104:
	v_cvt_pk_bf16_f32 v96, v96, v97
	v_cvt_pk_bf16_f32 v97, v98, v99
	v_add_u32_e32 v98, s17, v154
	global_store_dwordx2 v[114:115], v[96:97], off offset:288
	v_lshlrev_b32_e32 v96, 4, v98
	v_cvt_pk_bf16_f32 v100, v100, v101
	v_cvt_pk_bf16_f32 v101, v102, v103
	s_and_b64 vcc, exec, s[6:7]
	v_ashrrev_i32_e32 v97, 31, v96
	global_store_dwordx2 v[114:115], v[100:101], off offset:256
	s_cbranch_vccnz .LBB0_108
	s_add_i32 s2, s15, 0xfffffa00
	s_cmpk_lt_u32 s2, 0x280
	v_cmp_gt_i32_e32 vcc, s47, v144
	s_cselect_b64 s[2:3], -1, 0
	s_or_b64 s[34:35], vcc, s[2:3]
	s_and_saveexec_b64 s[2:3], s[34:35]
	s_cbranch_execz .LBB0_107
	v_lshl_add_u64 v[104:105], v[96:97], 2, v[134:135]
	s_nop 0
	v_mov_b32_e32 v112, v94
	v_mov_b32_e32 v113, v94
	v_mov_b32_e32 v99, v92
	v_mov_b32_e32 v109, v92
	v_mov_b32_e32 v110, v93
	v_mov_b32_e32 v111, v93
	v_mov_b32_e32 v114, v95
	v_mov_b32_e32 v115, v95
	v_mov_b32_e32 v108, v95
	s_nop 1
	v_permlane32_swap_b32 v112, v113
	s_nop 1
	v_permlane32_swap_b32 v99, v109
	s_nop 1
	v_permlane32_swap_b32 v110, v111
	s_nop 1
	v_permlane32_swap_b32 v114, v115
	v_mov_b32_e32 v104, v196
	v_mov_b32_e32 v105, v197
	v_mov_b32_e32 v106, v198
	v_mov_b32_e32 v107, v199
	v_mov_b32_e32 v100, v200
	v_mov_b32_e32 v101, v201
	v_mov_b32_e32 v102, v202
	v_mov_b32_e32 v103, v203
	v_mul_f32_e32 v94, v94, v106
	v_cndmask_b32_e64 v95, v113, v112, s[0:1]
	v_cndmask_b32_e64 v112, v115, v114, s[0:1]
	v_mul_f32_e32 v95, v132, v95
	v_cndmask_b32_e64 v111, v111, v110, s[0:1]
	v_cndmask_b32_e64 v110, v109, v99, s[0:1]
	v_mul_f32_e32 v109, v132, v112
	v_mul_f32_e32 v106, v102, v95
	v_mov_b32_e32 v102, v107
	v_pk_mul_f32 v[110:111], v[132:133], v[110:111]
	v_pk_mul_f32 v[102:103], v[108:109], v[102:103]
	v_pk_mul_f32 v[100:101], v[100:101], v[110:111]
	v_mov_b32_e32 v95, v102
	v_mov_b32_e32 v107, v103
	v_pk_fma_f32 v[92:93], v[92:93], v[104:105], v[100:101]
	v_pk_add_f32 v[94:95], v[94:95], v[106:107]

.LBB0_108:
	v_readlane_b32 s2, v253, 22
	v_readlane_b32 s3, v253, 23
	v_cvt_pk_bf16_f32 v92, v92, v93
	v_cvt_pk_bf16_f32 v93, v94, v95
	v_mov_b64_e32 v[100:101], s[2:3]
	v_mad_i64_i32 v[98:99], s[2:3], v98, s55, v[100:101]
	v_lshl_add_u64 v[98:99], v[144:145], 1, v[98:99]
	v_cvt_pk_bf16_f32 v88, v88, v89
	v_cvt_pk_bf16_f32 v89, v90, v91
	s_and_b64 vcc, exec, s[6:7]
	global_store_dwordx2 v[98:99], v[92:93], off
	global_store_dwordx2 v[98:99], v[88:89], off offset:32
	s_cbranch_vccnz .LBB0_112
	s_add_i32 s2, s15, 0xfffffa80
	s_cmpk_lt_u32 s2, 0x280
	v_cmp_gt_i32_e32 vcc, s47, v120
	s_cselect_b64 s[2:3], -1, 0
	s_or_b64 s[34:35], vcc, s[2:3]
	s_and_saveexec_b64 s[2:3], s[34:35]
	s_cbranch_execz .LBB0_111
	v_lshl_add_u64 v[92:93], v[96:97], 2, v[134:135]
	s_nop 0
	v_mov_b32_e32 v103, v86
	v_mov_b32_e32 v104, v86
	v_mov_b32_e32 v97, v84
	v_mov_b32_e32 v100, v84
	v_mov_b32_e32 v101, v85
	v_mov_b32_e32 v102, v85
	v_mov_b32_e32 v105, v87
	v_mov_b32_e32 v106, v87
	v_mov_b32_e32 v96, v87
	s_nop 1
	v_permlane32_swap_b32 v103, v104
	s_nop 1
	v_permlane32_swap_b32 v97, v100
	s_nop 1
	v_permlane32_swap_b32 v101, v102
	s_nop 1
	v_permlane32_swap_b32 v105, v106
	v_mov_b32_e32 v92, v196
	v_mov_b32_e32 v93, v197
	v_mov_b32_e32 v94, v198
	v_mov_b32_e32 v95, v199
	v_mov_b32_e32 v88, v200
	v_mov_b32_e32 v89, v201
	v_mov_b32_e32 v90, v202
	v_mov_b32_e32 v91, v203
	v_mul_f32_e32 v86, v86, v94
	v_cndmask_b32_e64 v87, v104, v103, s[0:1]
	v_cndmask_b32_e64 v103, v106, v105, s[0:1]
	v_mul_f32_e32 v87, v132, v87
	v_cndmask_b32_e64 v101, v102, v101, s[0:1]
	v_cndmask_b32_e64 v100, v100, v97, s[0:1]
	v_mul_f32_e32 v97, v132, v103
	v_mul_f32_e32 v94, v90, v87
	v_mov_b32_e32 v90, v95
	v_pk_mul_f32 v[100:101], v[132:133], v[100:101]
	v_pk_mul_f32 v[90:91], v[96:97], v[90:91]
	v_pk_mul_f32 v[88:89], v[88:89], v[100:101]
	v_mov_b32_e32 v87, v90
	v_mov_b32_e32 v95, v91
	v_pk_fma_f32 v[84:85], v[84:85], v[92:93], v[88:89]
	v_pk_add_f32 v[86:87], v[86:87], v[94:95]

.LBB0_112:
	v_cvt_pk_bf16_f32 v80, v80, v81
	v_cvt_pk_bf16_f32 v81, v82, v83
	v_add_u32_e32 v82, s17, v155
	global_store_dwordx2 v[98:99], v[80:81], off offset:288
	v_lshlrev_b32_e32 v80, 4, v82
	v_cvt_pk_bf16_f32 v84, v84, v85
	v_cvt_pk_bf16_f32 v85, v86, v87
	s_and_b64 vcc, exec, s[6:7]
	v_ashrrev_i32_e32 v81, 31, v80
	global_store_dwordx2 v[98:99], v[84:85], off offset:256
	s_cbranch_vccnz .LBB0_116
	s_add_i32 s2, s15, 0xfffffa00
	s_cmpk_lt_u32 s2, 0x280
	v_cmp_gt_i32_e32 vcc, s47, v144
	s_cselect_b64 s[2:3], -1, 0
	s_or_b64 s[34:35], vcc, s[2:3]
	s_and_saveexec_b64 s[2:3], s[34:35]
	s_cbranch_execz .LBB0_115
	v_lshl_add_u64 v[88:89], v[80:81], 2, v[134:135]
	s_nop 0
	v_mov_b32_e32 v96, v78
	v_mov_b32_e32 v97, v78
	v_mov_b32_e32 v83, v76
	v_mov_b32_e32 v93, v76
	v_mov_b32_e32 v94, v77
	v_mov_b32_e32 v95, v77
	v_mov_b32_e32 v98, v79
	v_mov_b32_e32 v99, v79
	v_mov_b32_e32 v92, v79
	s_nop 1
	v_permlane32_swap_b32 v96, v97
	s_nop 1
	v_permlane32_swap_b32 v83, v93
	s_nop 1
	v_permlane32_swap_b32 v94, v95
	s_nop 1
	v_permlane32_swap_b32 v98, v99
	v_mov_b32_e32 v88, v204
	v_mov_b32_e32 v89, v205
	v_mov_b32_e32 v90, v206
	v_mov_b32_e32 v91, v207
	v_mov_b32_e32 v84, v208
	v_mov_b32_e32 v85, v209
	v_mov_b32_e32 v86, v210
	v_mov_b32_e32 v87, v211
	v_mul_f32_e32 v78, v78, v90
	v_cndmask_b32_e64 v79, v97, v96, s[0:1]
	v_cndmask_b32_e64 v96, v99, v98, s[0:1]
	v_mul_f32_e32 v79, v132, v79
	v_cndmask_b32_e64 v95, v95, v94, s[0:1]
	v_cndmask_b32_e64 v94, v93, v83, s[0:1]
	v_mul_f32_e32 v93, v132, v96
	v_mul_f32_e32 v90, v86, v79
	v_mov_b32_e32 v86, v91
	v_pk_mul_f32 v[94:95], v[132:133], v[94:95]
	v_pk_mul_f32 v[86:87], v[92:93], v[86:87]
	v_pk_mul_f32 v[84:85], v[84:85], v[94:95]
	v_mov_b32_e32 v79, v86
	v_mov_b32_e32 v91, v87
	v_pk_fma_f32 v[76:77], v[76:77], v[88:89], v[84:85]
	v_pk_add_f32 v[78:79], v[78:79], v[90:91]

.LBB0_116:
	v_readlane_b32 s2, v253, 22
	v_readlane_b32 s3, v253, 23
	v_cvt_pk_bf16_f32 v76, v76, v77
	v_cvt_pk_bf16_f32 v77, v78, v79
	v_mov_b64_e32 v[84:85], s[2:3]
	v_mad_i64_i32 v[82:83], s[2:3], v82, s55, v[84:85]
	v_lshl_add_u64 v[82:83], v[144:145], 1, v[82:83]
	v_cvt_pk_bf16_f32 v72, v72, v73
	v_cvt_pk_bf16_f32 v73, v74, v75
	s_and_b64 vcc, exec, s[6:7]
	global_store_dwordx2 v[82:83], v[76:77], off
	global_store_dwordx2 v[82:83], v[72:73], off offset:32
	s_cbranch_vccnz .LBB0_120
	s_add_i32 s2, s15, 0xfffffa80
	s_cmpk_lt_u32 s2, 0x280
	v_cmp_gt_i32_e32 vcc, s47, v120
	s_cselect_b64 s[2:3], -1, 0
	s_or_b64 s[34:35], vcc, s[2:3]
	s_and_saveexec_b64 s[2:3], s[34:35]
	s_cbranch_execz .LBB0_119
	v_lshl_add_u64 v[76:77], v[80:81], 2, v[134:135]
	s_nop 0
	v_mov_b32_e32 v87, v70
	v_mov_b32_e32 v88, v70
	v_mov_b32_e32 v81, v68
	v_mov_b32_e32 v84, v68
	v_mov_b32_e32 v85, v69
	v_mov_b32_e32 v86, v69
	v_mov_b32_e32 v89, v71
	v_mov_b32_e32 v90, v71
	v_mov_b32_e32 v80, v71
	s_nop 1
	v_permlane32_swap_b32 v87, v88
	s_nop 1
	v_permlane32_swap_b32 v81, v84
	s_nop 1
	v_permlane32_swap_b32 v85, v86
	s_nop 1
	v_permlane32_swap_b32 v89, v90
	v_mov_b32_e32 v76, v204
	v_mov_b32_e32 v77, v205
	v_mov_b32_e32 v78, v206
	v_mov_b32_e32 v79, v207
	v_mov_b32_e32 v72, v208
	v_mov_b32_e32 v73, v209
	v_mov_b32_e32 v74, v210
	v_mov_b32_e32 v75, v211
	v_mul_f32_e32 v70, v70, v78
	v_cndmask_b32_e64 v71, v88, v87, s[0:1]
	v_cndmask_b32_e64 v87, v90, v89, s[0:1]
	v_mul_f32_e32 v71, v132, v71
	v_cndmask_b32_e64 v85, v86, v85, s[0:1]
	v_cndmask_b32_e64 v84, v84, v81, s[0:1]
	v_mul_f32_e32 v81, v132, v87
	v_mul_f32_e32 v78, v74, v71
	v_mov_b32_e32 v74, v79
	v_pk_mul_f32 v[84:85], v[132:133], v[84:85]
	v_pk_mul_f32 v[74:75], v[80:81], v[74:75]
	v_pk_mul_f32 v[72:73], v[72:73], v[84:85]
	v_mov_b32_e32 v71, v74
	v_mov_b32_e32 v79, v75
	v_pk_fma_f32 v[68:69], v[68:69], v[76:77], v[72:73]
	v_pk_add_f32 v[70:71], v[70:71], v[78:79]

.LBB0_120:
	v_cvt_pk_bf16_f32 v64, v64, v65
	v_cvt_pk_bf16_f32 v65, v66, v67
	v_add_u32_e32 v66, s17, v156
	global_store_dwordx2 v[82:83], v[64:65], off offset:288
	v_lshlrev_b32_e32 v64, 4, v66
	v_cvt_pk_bf16_f32 v68, v68, v69
	v_cvt_pk_bf16_f32 v69, v70, v71
	s_and_b64 vcc, exec, s[6:7]
	v_ashrrev_i32_e32 v65, 31, v64
	global_store_dwordx2 v[82:83], v[68:69], off offset:256
	s_cbranch_vccnz .LBB0_124
	s_add_i32 s2, s15, 0xfffffa00
	s_cmpk_lt_u32 s2, 0x280
	v_cmp_gt_i32_e32 vcc, s47, v144
	s_cselect_b64 s[2:3], -1, 0
	s_or_b64 s[34:35], vcc, s[2:3]
	s_and_saveexec_b64 s[2:3], s[34:35]
	s_cbranch_execz .LBB0_123
	v_lshl_add_u64 v[72:73], v[64:65], 2, v[134:135]
	s_nop 0
	v_mov_b32_e32 v80, v62
	v_mov_b32_e32 v81, v62
	v_mov_b32_e32 v67, v60
	v_mov_b32_e32 v77, v60
	v_mov_b32_e32 v78, v61
	v_mov_b32_e32 v79, v61
	v_mov_b32_e32 v82, v63
	v_mov_b32_e32 v83, v63
	v_mov_b32_e32 v76, v63
	s_nop 1
	v_permlane32_swap_b32 v81, v80
	s_nop 1
	v_permlane32_swap_b32 v77, v67
	s_nop 1
	v_permlane32_swap_b32 v79, v78
	s_nop 1
	v_permlane32_swap_b32 v83, v82
	v_mov_b32_e32 v72, v212
	v_mov_b32_e32 v73, v213
	v_mov_b32_e32 v74, v214
	v_mov_b32_e32 v75, v215
	v_mov_b32_e32 v68, v216
	v_mov_b32_e32 v69, v217
	v_mov_b32_e32 v70, v218
	v_mov_b32_e32 v71, v219
	v_mul_f32_e32 v62, v62, v74
	v_cndmask_b32_e64 v63, v80, v81, s[0:1]
	v_cndmask_b32_e64 v80, v82, v83, s[0:1]
	v_mul_f32_e32 v63, v132, v63
	v_cndmask_b32_e64 v79, v78, v79, s[0:1]
	v_cndmask_b32_e64 v78, v67, v77, s[0:1]
	v_mul_f32_e32 v77, v132, v80
	v_mul_f32_e32 v74, v70, v63
	v_mov_b32_e32 v70, v75
	v_pk_mul_f32 v[78:79], v[132:133], v[78:79]
	v_pk_mul_f32 v[70:71], v[76:77], v[70:71]
	v_pk_mul_f32 v[68:69], v[68:69], v[78:79]
	v_mov_b32_e32 v63, v70
	v_mov_b32_e32 v75, v71
	v_pk_fma_f32 v[60:61], v[60:61], v[72:73], v[68:69]
	v_pk_add_f32 v[62:63], v[62:63], v[74:75]

.LBB0_124:
	v_readlane_b32 s2, v253, 22
	v_readlane_b32 s3, v253, 23
	v_cvt_pk_bf16_f32 v60, v60, v61
	v_cvt_pk_bf16_f32 v61, v62, v63
	v_mov_b64_e32 v[68:69], s[2:3]
	v_mad_i64_i32 v[66:67], s[2:3], v66, s55, v[68:69]
	v_lshl_add_u64 v[66:67], v[144:145], 1, v[66:67]
	v_cvt_pk_bf16_f32 v56, v56, v57
	v_cvt_pk_bf16_f32 v57, v58, v59
	s_and_b64 vcc, exec, s[6:7]
	global_store_dwordx2 v[66:67], v[60:61], off
	global_store_dwordx2 v[66:67], v[56:57], off offset:32
	s_cbranch_vccnz .LBB0_128
	s_add_i32 s2, s15, 0xfffffa80
	s_cmpk_lt_u32 s2, 0x280
	v_cmp_gt_i32_e32 vcc, s47, v120
	s_cselect_b64 s[2:3], -1, 0
	s_or_b64 s[34:35], vcc, s[2:3]
	s_and_saveexec_b64 s[2:3], s[34:35]
	s_cbranch_execz .LBB0_127
	v_lshl_add_u64 v[60:61], v[64:65], 2, v[134:135]
	s_nop 0
	v_mov_b32_e32 v71, v54
	v_mov_b32_e32 v72, v54
	v_mov_b32_e32 v65, v52
	v_mov_b32_e32 v68, v52
	v_mov_b32_e32 v69, v53
	v_mov_b32_e32 v70, v53
	v_mov_b32_e32 v73, v55
	v_mov_b32_e32 v74, v55
	v_mov_b32_e32 v64, v55
	s_nop 1
	v_permlane32_swap_b32 v72, v71
	s_nop 1
	v_permlane32_swap_b32 v68, v65
	s_nop 1
	v_permlane32_swap_b32 v70, v69
	s_nop 1
	v_permlane32_swap_b32 v74, v73
	v_mov_b32_e32 v60, v212
	v_mov_b32_e32 v61, v213
	v_mov_b32_e32 v62, v214
	v_mov_b32_e32 v63, v215
	v_mov_b32_e32 v56, v216
	v_mov_b32_e32 v57, v217
	v_mov_b32_e32 v58, v218
	v_mov_b32_e32 v59, v219
	v_mul_f32_e32 v54, v54, v62
	v_cndmask_b32_e64 v55, v71, v72, s[0:1]
	v_cndmask_b32_e64 v71, v73, v74, s[0:1]
	v_mul_f32_e32 v55, v132, v55
	v_cndmask_b32_e64 v69, v69, v70, s[0:1]
	v_cndmask_b32_e64 v68, v65, v68, s[0:1]
	v_mul_f32_e32 v65, v132, v71
	v_mul_f32_e32 v62, v58, v55
	v_mov_b32_e32 v58, v63
	v_pk_mul_f32 v[68:69], v[132:133], v[68:69]
	v_pk_mul_f32 v[58:59], v[64:65], v[58:59]
	v_pk_mul_f32 v[56:57], v[56:57], v[68:69]
	v_mov_b32_e32 v55, v58
	v_mov_b32_e32 v63, v59
	v_pk_fma_f32 v[52:53], v[52:53], v[60:61], v[56:57]
	v_pk_add_f32 v[54:55], v[54:55], v[62:63]

.LBB0_128:
	v_cvt_pk_bf16_f32 v48, v48, v49
	v_cvt_pk_bf16_f32 v49, v50, v51
	v_add_u32_e32 v50, s17, v157
	global_store_dwordx2 v[66:67], v[48:49], off offset:288
	v_lshlrev_b32_e32 v48, 4, v50
	v_cvt_pk_bf16_f32 v52, v52, v53
	v_cvt_pk_bf16_f32 v53, v54, v55
	s_and_b64 vcc, exec, s[6:7]
	v_ashrrev_i32_e32 v49, 31, v48
	global_store_dwordx2 v[66:67], v[52:53], off offset:256
	s_cbranch_vccnz .LBB0_132
	s_add_i32 s2, s15, 0xfffffa00
	s_cmpk_lt_u32 s2, 0x280
	v_cmp_gt_i32_e32 vcc, s47, v144
	s_cselect_b64 s[2:3], -1, 0
	s_or_b64 s[34:35], vcc, s[2:3]
	s_and_saveexec_b64 s[2:3], s[34:35]
	s_cbranch_execz .LBB0_131
	v_lshl_add_u64 v[56:57], v[48:49], 2, v[134:135]
	s_nop 0
	v_mov_b32_e32 v64, v46
	v_mov_b32_e32 v65, v46
	v_mov_b32_e32 v51, v44
	v_mov_b32_e32 v61, v44
	v_mov_b32_e32 v62, v45
	v_mov_b32_e32 v63, v45
	v_mov_b32_e32 v66, v47
	v_mov_b32_e32 v67, v47
	v_mov_b32_e32 v60, v47
	s_nop 1
	v_permlane32_swap_b32 v64, v65
	s_nop 1
	v_permlane32_swap_b32 v51, v61
	s_nop 1
	v_permlane32_swap_b32 v62, v63
	s_nop 1
	v_permlane32_swap_b32 v66, v67
	v_mov_b32_e32 v56, v220
	v_mov_b32_e32 v57, v221
	v_mov_b32_e32 v58, v222
	v_mov_b32_e32 v59, v223
	v_mov_b32_e32 v52, v232
	v_mov_b32_e32 v53, v233
	v_mov_b32_e32 v54, v234
	v_mov_b32_e32 v55, v235
	v_mul_f32_e32 v46, v46, v58
	v_cndmask_b32_e64 v47, v65, v64, s[0:1]
	v_cndmask_b32_e64 v64, v67, v66, s[0:1]
	v_mul_f32_e32 v47, v132, v47
	v_cndmask_b32_e64 v63, v63, v62, s[0:1]
	v_cndmask_b32_e64 v62, v61, v51, s[0:1]
	v_mul_f32_e32 v61, v132, v64
	v_mul_f32_e32 v58, v54, v47
	v_mov_b32_e32 v54, v59
	v_pk_mul_f32 v[62:63], v[132:133], v[62:63]
	v_pk_mul_f32 v[54:55], v[60:61], v[54:55]
	v_pk_mul_f32 v[52:53], v[52:53], v[62:63]
	v_mov_b32_e32 v47, v54
	v_mov_b32_e32 v59, v55
	v_pk_fma_f32 v[44:45], v[44:45], v[56:57], v[52:53]
	v_pk_add_f32 v[46:47], v[46:47], v[58:59]

.LBB0_132:
	v_readlane_b32 s2, v253, 22
	v_readlane_b32 s3, v253, 23
	v_cvt_pk_bf16_f32 v44, v44, v45
	v_cvt_pk_bf16_f32 v45, v46, v47
	v_mov_b64_e32 v[52:53], s[2:3]
	v_mad_i64_i32 v[50:51], s[2:3], v50, s55, v[52:53]
	v_lshl_add_u64 v[50:51], v[144:145], 1, v[50:51]
	v_cvt_pk_bf16_f32 v40, v40, v41
	v_cvt_pk_bf16_f32 v41, v42, v43
	s_and_b64 vcc, exec, s[6:7]
	global_store_dwordx2 v[50:51], v[44:45], off
	global_store_dwordx2 v[50:51], v[40:41], off offset:32
	s_cbranch_vccnz .LBB0_136
	s_add_i32 s2, s15, 0xfffffa80
	s_cmpk_lt_u32 s2, 0x280
	v_cmp_gt_i32_e32 vcc, s47, v120
	s_cselect_b64 s[2:3], -1, 0
	s_or_b64 s[34:35], vcc, s[2:3]
	s_and_saveexec_b64 s[2:3], s[34:35]
	s_cbranch_execz .LBB0_135
	v_lshl_add_u64 v[44:45], v[48:49], 2, v[134:135]
	s_nop 0
	v_mov_b32_e32 v55, v38
	v_mov_b32_e32 v56, v38
	v_mov_b32_e32 v49, v36
	v_mov_b32_e32 v52, v36
	v_mov_b32_e32 v53, v37
	v_mov_b32_e32 v54, v37
	v_mov_b32_e32 v57, v39
	v_mov_b32_e32 v58, v39
	v_mov_b32_e32 v48, v39
	s_nop 1
	v_permlane32_swap_b32 v55, v56
	s_nop 1
	v_permlane32_swap_b32 v49, v52
	s_nop 1
	v_permlane32_swap_b32 v53, v54
	s_nop 1
	v_permlane32_swap_b32 v57, v58
	v_mov_b32_e32 v44, v220
	v_mov_b32_e32 v45, v221
	v_mov_b32_e32 v46, v222
	v_mov_b32_e32 v47, v223
	v_mov_b32_e32 v40, v232
	v_mov_b32_e32 v41, v233
	v_mov_b32_e32 v42, v234
	v_mov_b32_e32 v43, v235
	v_mul_f32_e32 v38, v38, v46
	v_cndmask_b32_e64 v39, v56, v55, s[0:1]
	v_cndmask_b32_e64 v55, v58, v57, s[0:1]
	v_mul_f32_e32 v39, v132, v39
	v_cndmask_b32_e64 v53, v54, v53, s[0:1]
	v_cndmask_b32_e64 v52, v52, v49, s[0:1]
	v_mul_f32_e32 v49, v132, v55
	v_mul_f32_e32 v46, v42, v39
	v_mov_b32_e32 v42, v47
	v_pk_mul_f32 v[52:53], v[132:133], v[52:53]
	v_pk_mul_f32 v[42:43], v[48:49], v[42:43]
	v_pk_mul_f32 v[40:41], v[40:41], v[52:53]
	v_mov_b32_e32 v39, v42
	v_mov_b32_e32 v47, v43
	v_pk_fma_f32 v[36:37], v[36:37], v[44:45], v[40:41]
	v_pk_add_f32 v[38:39], v[38:39], v[46:47]

.LBB0_136:
	v_cvt_pk_bf16_f32 v32, v32, v33
	v_cvt_pk_bf16_f32 v33, v34, v35
	v_add_u32_e32 v34, s17, v158
	global_store_dwordx2 v[50:51], v[32:33], off offset:288
	v_lshlrev_b32_e32 v32, 4, v34
	v_cvt_pk_bf16_f32 v36, v36, v37
	v_cvt_pk_bf16_f32 v37, v38, v39
	s_and_b64 vcc, exec, s[6:7]
	v_ashrrev_i32_e32 v33, 31, v32
	global_store_dwordx2 v[50:51], v[36:37], off offset:256
	s_cbranch_vccnz .LBB0_140
	s_add_i32 s2, s15, 0xfffffa00
	s_cmpk_lt_u32 s2, 0x280
	v_cmp_gt_i32_e32 vcc, s47, v144
	s_cselect_b64 s[2:3], -1, 0
	s_or_b64 s[34:35], vcc, s[2:3]
	s_and_saveexec_b64 s[2:3], s[34:35]
	s_cbranch_execz .LBB0_139
	v_lshl_add_u64 v[40:41], v[32:33], 2, v[134:135]
	s_nop 0
	v_mov_b32_e32 v48, v30
	v_mov_b32_e32 v49, v30
	v_mov_b32_e32 v35, v28
	v_mov_b32_e32 v45, v28
	v_mov_b32_e32 v46, v29
	v_mov_b32_e32 v47, v29
	v_mov_b32_e32 v50, v31
	v_mov_b32_e32 v51, v31
	v_mov_b32_e32 v44, v31
	s_nop 1
	v_permlane32_swap_b32 v48, v49
	s_nop 1
	v_permlane32_swap_b32 v35, v45
	s_nop 1
	v_permlane32_swap_b32 v46, v47
	s_nop 1
	v_permlane32_swap_b32 v50, v51
	v_mov_b32_e32 v40, v236
	v_mov_b32_e32 v41, v237
	v_mov_b32_e32 v42, v238
	v_mov_b32_e32 v43, v239
	v_mov_b32_e32 v36, v240
	v_mov_b32_e32 v37, v241
	v_mov_b32_e32 v38, v242
	v_mov_b32_e32 v39, v243
	v_mul_f32_e32 v30, v30, v42
	v_cndmask_b32_e64 v31, v49, v48, s[0:1]
	v_cndmask_b32_e64 v48, v51, v50, s[0:1]
	v_mul_f32_e32 v31, v132, v31
	v_cndmask_b32_e64 v47, v47, v46, s[0:1]
	v_cndmask_b32_e64 v46, v45, v35, s[0:1]
	v_mul_f32_e32 v45, v132, v48
	v_mul_f32_e32 v42, v38, v31
	v_mov_b32_e32 v38, v43
	v_pk_mul_f32 v[46:47], v[132:133], v[46:47]
	v_pk_mul_f32 v[38:39], v[44:45], v[38:39]
	v_pk_mul_f32 v[36:37], v[36:37], v[46:47]
	v_mov_b32_e32 v31, v38
	v_mov_b32_e32 v43, v39
	v_pk_fma_f32 v[28:29], v[28:29], v[40:41], v[36:37]
	v_pk_add_f32 v[30:31], v[30:31], v[42:43]

.LBB0_140:
	v_readlane_b32 s2, v253, 22
	v_readlane_b32 s3, v253, 23
	v_cvt_pk_bf16_f32 v28, v28, v29
	v_cvt_pk_bf16_f32 v29, v30, v31
	v_mov_b64_e32 v[36:37], s[2:3]
	v_mad_i64_i32 v[34:35], s[2:3], v34, s55, v[36:37]
	v_lshl_add_u64 v[34:35], v[144:145], 1, v[34:35]
	v_cvt_pk_bf16_f32 v24, v24, v25
	v_cvt_pk_bf16_f32 v25, v26, v27
	s_and_b64 vcc, exec, s[6:7]
	global_store_dwordx2 v[34:35], v[28:29], off
	global_store_dwordx2 v[34:35], v[24:25], off offset:32
	s_cbranch_vccnz .LBB0_144
	s_add_i32 s2, s15, 0xfffffa80
	s_cmpk_lt_u32 s2, 0x280
	v_cmp_gt_i32_e32 vcc, s47, v120
	s_cselect_b64 s[2:3], -1, 0
	s_or_b64 s[34:35], vcc, s[2:3]
	s_and_saveexec_b64 s[2:3], s[34:35]
	s_cbranch_execz .LBB0_143
	v_lshl_add_u64 v[28:29], v[32:33], 2, v[134:135]
	s_nop 0
	v_mov_b32_e32 v39, v22
	v_mov_b32_e32 v40, v22
	v_mov_b32_e32 v33, v20
	v_mov_b32_e32 v36, v20
	v_mov_b32_e32 v37, v21
	v_mov_b32_e32 v38, v21
	v_mov_b32_e32 v41, v23
	v_mov_b32_e32 v42, v23
	v_mov_b32_e32 v32, v23
	s_nop 1
	v_permlane32_swap_b32 v39, v40
	s_nop 1
	v_permlane32_swap_b32 v33, v36
	s_nop 1
	v_permlane32_swap_b32 v37, v38
	s_nop 1
	v_permlane32_swap_b32 v41, v42
	v_mov_b32_e32 v28, v236
	v_mov_b32_e32 v29, v237
	v_mov_b32_e32 v30, v238
	v_mov_b32_e32 v31, v239
	v_mov_b32_e32 v24, v240
	v_mov_b32_e32 v25, v241
	v_mov_b32_e32 v26, v242
	v_mov_b32_e32 v27, v243
	v_mul_f32_e32 v22, v22, v30
	v_cndmask_b32_e64 v23, v40, v39, s[0:1]
	v_cndmask_b32_e64 v39, v42, v41, s[0:1]
	v_mul_f32_e32 v23, v132, v23
	v_cndmask_b32_e64 v37, v38, v37, s[0:1]
	v_cndmask_b32_e64 v36, v36, v33, s[0:1]
	v_mul_f32_e32 v33, v132, v39
	v_mul_f32_e32 v30, v26, v23
	v_mov_b32_e32 v26, v31
	v_pk_mul_f32 v[36:37], v[132:133], v[36:37]
	v_pk_mul_f32 v[26:27], v[32:33], v[26:27]
	v_pk_mul_f32 v[24:25], v[24:25], v[36:37]
	v_mov_b32_e32 v23, v26
	v_mov_b32_e32 v31, v27
	v_pk_fma_f32 v[20:21], v[20:21], v[28:29], v[24:25]
	v_pk_add_f32 v[22:23], v[22:23], v[30:31]

.LBB0_144:
	v_cvt_pk_bf16_f32 v16, v16, v17
	v_cvt_pk_bf16_f32 v17, v18, v19
	v_add_u32_e32 v18, s17, v159
	global_store_dwordx2 v[34:35], v[16:17], off offset:288
	v_lshlrev_b32_e32 v16, 4, v18
	v_cvt_pk_bf16_f32 v20, v20, v21
	v_cvt_pk_bf16_f32 v21, v22, v23
	s_and_b64 vcc, exec, s[6:7]
	v_ashrrev_i32_e32 v17, 31, v16
	global_store_dwordx2 v[34:35], v[20:21], off offset:256
	s_cbranch_vccnz .LBB0_148
	s_add_i32 s2, s15, 0xfffffa00
	s_cmpk_lt_u32 s2, 0x280
	v_cmp_gt_i32_e32 vcc, s47, v144
	s_cselect_b64 s[2:3], -1, 0
	s_or_b64 s[34:35], vcc, s[2:3]
	s_and_saveexec_b64 s[2:3], s[34:35]
	s_cbranch_execz .LBB0_147
	v_lshl_add_u64 v[24:25], v[16:17], 2, v[134:135]
	s_nop 0
	v_mov_b32_e32 v32, v14
	v_mov_b32_e32 v33, v14
	v_mov_b32_e32 v19, v12
	v_mov_b32_e32 v29, v12
	v_mov_b32_e32 v30, v13
	v_mov_b32_e32 v31, v13
	v_mov_b32_e32 v34, v15
	v_mov_b32_e32 v35, v15
	v_mov_b32_e32 v28, v15
	s_nop 1
	v_permlane32_swap_b32 v32, v33
	s_nop 1
	v_permlane32_swap_b32 v19, v29
	s_nop 1
	v_permlane32_swap_b32 v30, v31
	s_nop 1
	v_permlane32_swap_b32 v34, v35
	v_mov_b32_e32 v24, v244
	v_mov_b32_e32 v25, v245
	v_mov_b32_e32 v26, v246
	v_mov_b32_e32 v27, v247
	v_mov_b32_e32 v20, v248
	v_mov_b32_e32 v21, v249
	v_mov_b32_e32 v22, v250
	v_mov_b32_e32 v23, v251
	v_mul_f32_e32 v14, v14, v26
	v_cndmask_b32_e64 v15, v33, v32, s[0:1]
	v_cndmask_b32_e64 v32, v35, v34, s[0:1]
	v_mul_f32_e32 v15, v132, v15
	v_cndmask_b32_e64 v31, v31, v30, s[0:1]
	v_cndmask_b32_e64 v30, v29, v19, s[0:1]
	v_mul_f32_e32 v29, v132, v32
	v_mul_f32_e32 v26, v22, v15
	v_mov_b32_e32 v22, v27
	v_pk_mul_f32 v[30:31], v[132:133], v[30:31]
	v_pk_mul_f32 v[22:23], v[28:29], v[22:23]
	v_pk_mul_f32 v[20:21], v[20:21], v[30:31]
	v_mov_b32_e32 v15, v22
	v_mov_b32_e32 v27, v23
	v_pk_fma_f32 v[12:13], v[12:13], v[24:25], v[20:21]
	v_pk_add_f32 v[14:15], v[14:15], v[26:27]

.LBB0_148:
	v_readlane_b32 s2, v253, 22
	v_readlane_b32 s3, v253, 23
	v_cvt_pk_bf16_f32 v12, v12, v13
	v_cvt_pk_bf16_f32 v13, v14, v15
	v_mov_b64_e32 v[20:21], s[2:3]
	v_mad_i64_i32 v[18:19], s[2:3], v18, s55, v[20:21]
	v_lshl_add_u64 v[18:19], v[144:145], 1, v[18:19]
	v_cvt_pk_bf16_f32 v8, v8, v9
	v_cvt_pk_bf16_f32 v9, v10, v11
	s_and_b64 vcc, exec, s[6:7]
	global_store_dwordx2 v[18:19], v[12:13], off
	global_store_dwordx2 v[18:19], v[8:9], off offset:32
	s_cbranch_vccnz .LBB0_83
	s_addk_i32 s15, 0xfa80
	s_cmpk_lt_u32 s15, 0x280
	v_cmp_gt_i32_e32 vcc, s47, v120
	s_cselect_b64 s[2:3], -1, 0
	s_or_b64 s[6:7], vcc, s[2:3]
	s_and_saveexec_b64 s[2:3], s[6:7]
	s_cbranch_execz .LBB0_82
	v_lshl_add_u64 v[12:13], v[16:17], 2, v[134:135]
	s_nop 0
	v_mov_b32_e32 v23, v6
	v_mov_b32_e32 v24, v6
	v_mov_b32_e32 v17, v4
	v_mov_b32_e32 v20, v4
	v_mov_b32_e32 v21, v5
	v_mov_b32_e32 v22, v5
	v_mov_b32_e32 v25, v7
	v_mov_b32_e32 v26, v7
	v_mov_b32_e32 v16, v7
	s_nop 1
	v_permlane32_swap_b32 v23, v24
	s_nop 1
	v_permlane32_swap_b32 v17, v20
	s_nop 1
	v_permlane32_swap_b32 v21, v22
	s_nop 1
	v_permlane32_swap_b32 v25, v26
	v_mov_b32_e32 v12, v244
	v_mov_b32_e32 v13, v245
	v_mov_b32_e32 v14, v246
	v_mov_b32_e32 v15, v247
	v_mov_b32_e32 v8, v248
	v_mov_b32_e32 v9, v249
	v_mov_b32_e32 v10, v250
	v_mov_b32_e32 v11, v251
	v_mul_f32_e32 v6, v6, v14
	v_cndmask_b32_e64 v7, v24, v23, s[0:1]
	v_cndmask_b32_e64 v23, v26, v25, s[0:1]
	v_mul_f32_e32 v7, v132, v7
	v_cndmask_b32_e64 v21, v22, v21, s[0:1]
	v_cndmask_b32_e64 v20, v20, v17, s[0:1]
	v_mul_f32_e32 v17, v132, v23
	v_mul_f32_e32 v14, v10, v7
	v_mov_b32_e32 v10, v15
	v_pk_mul_f32 v[20:21], v[132:133], v[20:21]
	v_pk_mul_f32 v[10:11], v[16:17], v[10:11]
	v_pk_mul_f32 v[8:9], v[8:9], v[20:21]
	v_mov_b32_e32 v7, v10
	v_mov_b32_e32 v15, v11
	v_pk_fma_f32 v[4:5], v[4:5], v[12:13], v[8:9]
	v_pk_add_f32 v[6:7], v[6:7], v[14:15]
	s_branch .LBB0_82
